# baseline (speedup 1.0000x reference)
.Lk1_nodma24:
	v_cndmask_b32_e64 v30, 0, v30, s[18:19]
	v_cndmask_b32_e64 v31, 0, v31, s[18:19]
	v_cndmask_b32_e64 v32, 0, v32, s[18:19]
	v_cndmask_b32_e64 v33, 0, v33, s[18:19]
	v_max3_f32 v41, |v18|, |v19|, |v20|
	v_max3_f32 v42, |v21|, |v22|, |v23|
	v_max3_f32 v43, |v24|, |v25|, |v26|
	v_max3_f32 v44, |v27|, |v28|, |v29|
	v_max3_f32 v48, |v30|, |v31|, |v32|
	v_max3_f32 v41, v41, v42, |v33|
	v_max3_f32 v43, v43, v44, v48
	v_max_f32_e32 v41, v41, v43
	v_pk_add_f32 v[2:3], v[2:3], v[18:19]
	v_pk_add_f32 v[4:5], v[4:5], v[20:21]
	v_max_f32_dpp v41, v41, v41 quad_perm:[1,0,3,2] row_mask:0xf bank_mask:0xf
	v_pk_add_f32 v[6:7], v[6:7], v[22:23]
	v_pk_add_f32 v[8:9], v[8:9], v[24:25]
	v_max_f32_dpp v41, v41, v41 quad_perm:[2,3,0,1] row_mask:0xf bank_mask:0xf
	v_pk_add_f32 v[10:11], v[10:11], v[26:27]
	v_pk_add_f32 v[12:13], v[12:13], v[28:29]
	v_max_f32_dpp v41, v41, v41 row_half_mirror row_mask:0xf bank_mask:0xf
	v_pk_add_f32 v[14:15], v[14:15], v[30:31]
	v_pk_add_f32 v[16:17], v[16:17], v[32:33]
	v_max_f32_dpp v41, v41, v41 row_mirror row_mask:0xf bank_mask:0xf
	s_nop 1
	v_max_f32_dpp v41, v41, v41 row_bcast:15 row_mask:0xa bank_mask:0xf
	s_nop 1
	v_max_f32_dpp v41, v41, v41 row_bcast:31 row_mask:0xc bank_mask:0xf
	s_nop 1
	v_readlane_b32 s28, v41, 63
	s_nop 1
	v_div_scale_f32 v48, s[30:31], s28, s28, v47
	v_rcp_f32_e32 v49, v48
	s_nop 0
	v_fma_f32 v50, -v48, v49, 1.0
	v_fmac_f32_e32 v49, v50, v49
	v_mov_b32_e32 v50, s28
	v_div_scale_f32 v50, vcc, s32, v50, s32
	v_mul_f32_e32 v51, v50, v49
	v_fma_f32 v52, -v48, v51, v50
	v_fmac_f32_e32 v51, v52, v49
	v_fma_f32 v48, -v48, v51, v50
	v_div_fmas_f32 v48, v48, v49, v51
	v_div_fixup_f32 v48, v48, s28, v47
	v_cmp_gt_f32_e64 vcc, s28, 0
	v_writelane_b32 v40, s28, 23
	s_nop 0
	v_cndmask_b32_e32 v48, 0, v48, vcc
	v_fmaak_f32 v49, v18, v48, 0x4b400000
	v_fmaak_f32 v50, v19, v48, 0x4b400000
	v_fmaak_f32 v51, v20, v48, 0x4b400000
	v_fmaak_f32 v52, v21, v48, 0x4b400000
	v_perm_b32 v49, v50, v49, s33
	v_perm_b32 v51, v52, v51, s34
	v_or_b32_e32 v49, v49, v51
	ds_write_b32 v38, v49 offset:7168
	v_fmaak_f32 v41, v22, v48, 0x4b400000
	v_fmaak_f32 v42, v23, v48, 0x4b400000
	v_fmaak_f32 v43, v24, v48, 0x4b400000
	v_fmaak_f32 v44, v25, v48, 0x4b400000
	v_perm_b32 v41, v42, v41, s33
	v_perm_b32 v43, v44, v43, s34
	v_or_b32_e32 v41, v41, v43
	ds_write_b32 v38, v41 offset:7172
	v_fmaak_f32 v49, v26, v48, 0x4b400000
	v_fmaak_f32 v50, v27, v48, 0x4b400000
	v_fmaak_f32 v51, v28, v48, 0x4b400000
	v_fmaak_f32 v52, v29, v48, 0x4b400000
	v_perm_b32 v49, v50, v49, s33
	v_perm_b32 v51, v52, v51, s34
	v_or_b32_e32 v49, v49, v51
	ds_write_b32 v38, v49 offset:7176
	v_fmaak_f32 v41, v30, v48, 0x4b400000
	v_fmaak_f32 v42, v31, v48, 0x4b400000
	v_fmaak_f32 v43, v32, v48, 0x4b400000
	v_fmaak_f32 v44, v33, v48, 0x4b400000
	v_perm_b32 v41, v42, v41, s33
	v_perm_b32 v43, v44, v43, s34
	v_or_b32_e32 v41, v41, v43
	ds_write_b32 v38, v41 offset:7180
	s_cmp_eq_u32 s29, 1
	s_cbranch_scc0 .Lk1_flush
	s_waitcnt vmcnt(0)
	ds_read_b128 v[18:21], v38 offset:0
	ds_read_b128 v[22:25], v38 offset:1024
	ds_read_b128 v[26:29], v38 offset:2048
	ds_read_b128 v[30:33], v38 offset:3072
	s_waitcnt lgkmcnt(0)
	v_cndmask_b32_e64 v30, 0, v30, s[18:19]
	v_cndmask_b32_e64 v31, 0, v31, s[18:19]
	v_cndmask_b32_e64 v32, 0, v32, s[18:19]
	v_cndmask_b32_e64 v33, 0, v33, s[18:19]
	v_max3_f32 v41, |v18|, |v19|, |v20|
	v_max3_f32 v42, |v21|, |v22|, |v23|
	v_max3_f32 v43, |v24|, |v25|, |v26|
	v_max3_f32 v44, |v27|, |v28|, |v29|
	v_max3_f32 v48, |v30|, |v31|, |v32|
	v_max3_f32 v41, v41, v42, |v33|
	v_max3_f32 v43, v43, v44, v48
	v_max_f32_e32 v41, v41, v43
	v_pk_add_f32 v[2:3], v[2:3], v[18:19]
	v_pk_add_f32 v[4:5], v[4:5], v[20:21]
	v_max_f32_dpp v41, v41, v41 quad_perm:[1,0,3,2] row_mask:0xf bank_mask:0xf
	v_pk_add_f32 v[6:7], v[6:7], v[22:23]
	v_pk_add_f32 v[8:9], v[8:9], v[24:25]
	v_max_f32_dpp v41, v41, v41 quad_perm:[2,3,0,1] row_mask:0xf bank_mask:0xf
	v_pk_add_f32 v[10:11], v[10:11], v[26:27]
	v_pk_add_f32 v[12:13], v[12:13], v[28:29]
	v_max_f32_dpp v41, v41, v41 row_half_mirror row_mask:0xf bank_mask:0xf
	v_pk_add_f32 v[14:15], v[14:15], v[30:31]
	v_pk_add_f32 v[16:17], v[16:17], v[32:33]
	v_max_f32_dpp v41, v41, v41 row_mirror row_mask:0xf bank_mask:0xf
	s_nop 1
	v_max_f32_dpp v41, v41, v41 row_bcast:15 row_mask:0xa bank_mask:0xf
	s_nop 1
	v_max_f32_dpp v41, v41, v41 row_bcast:31 row_mask:0xc bank_mask:0xf
	s_nop 1
	v_readlane_b32 s28, v41, 63
	s_nop 1
	v_div_scale_f32 v48, s[30:31], s28, s28, v47
	v_rcp_f32_e32 v49, v48
	s_nop 0
	v_fma_f32 v50, -v48, v49, 1.0
	v_fmac_f32_e32 v49, v50, v49
	v_mov_b32_e32 v50, s28
	v_div_scale_f32 v50, vcc, s32, v50, s32
	v_mul_f32_e32 v51, v50, v49
	v_fma_f32 v52, -v48, v51, v50
	v_fmac_f32_e32 v51, v52, v49
	v_fma_f32 v48, -v48, v51, v50
	v_div_fmas_f32 v48, v48, v49, v51
	v_div_fixup_f32 v48, v48, s28, v47
	v_cmp_gt_f32_e64 vcc, s28, 0
	v_writelane_b32 v40, s28, 24
	s_nop 0
	v_cndmask_b32_e32 v48, 0, v48, vcc
	v_fmaak_f32 v49, v18, v48, 0x4b400000
	v_fmaak_f32 v50, v19, v48, 0x4b400000
	v_fmaak_f32 v51, v20, v48, 0x4b400000
	v_fmaak_f32 v52, v21, v48, 0x4b400000
	v_perm_b32 v49, v50, v49, s33
	v_perm_b32 v51, v52, v51, s34
	v_or_b32_e32 v18, v49, v51
	v_fmaak_f32 v41, v22, v48, 0x4b400000
	v_fmaak_f32 v42, v23, v48, 0x4b400000
	v_fmaak_f32 v43, v24, v48, 0x4b400000
	v_fmaak_f32 v44, v25, v48, 0x4b400000
	v_perm_b32 v41, v42, v41, s33
	v_perm_b32 v43, v44, v43, s34
	v_or_b32_e32 v19, v41, v43
	v_fmaak_f32 v49, v26, v48, 0x4b400000
	v_fmaak_f32 v50, v27, v48, 0x4b400000
	v_fmaak_f32 v51, v28, v48, 0x4b400000
	v_fmaak_f32 v52, v29, v48, 0x4b400000
	v_perm_b32 v49, v50, v49, s33
	v_perm_b32 v51, v52, v51, s34
	v_or_b32_e32 v20, v49, v51
	v_fmaak_f32 v41, v30, v48, 0x4b400000
	v_fmaak_f32 v42, v31, v48, 0x4b400000
	v_fmaak_f32 v43, v32, v48, 0x4b400000
	v_fmaak_f32 v44, v33, v48, 0x4b400000
	v_perm_b32 v41, v42, v41, s33
	v_perm_b32 v43, v44, v43, s34
	v_or_b32_e32 v21, v41, v43
.Lk1_flush:
	s_barrier
	s_add_u32 s20, s40, 0x0
	s_addc_u32 s21, s41, 0
	s_add_u32 s22, s20, 0x186a000
	s_addc_u32 s23, s21, 0
	s_add_u32 s24, s22, 0x186a000
	s_addc_u32 s25, s23, 0
	s_add_u32 s26, s24, 0x186a000
	s_addc_u32 s27, s25, 0
	global_store_dword v39, v56, s[20:21] sc1
	global_store_dword v39, v57, s[22:23] sc1
	global_store_dword v39, v58, s[24:25] sc1
	global_store_dword v39, v59, s[26:27] sc1
	s_add_u32 s20, s20, 0x80000
	s_addc_u32 s21, s21, 0
	s_add_u32 s22, s22, 0x80000
	s_addc_u32 s23, s23, 0
	s_add_u32 s24, s24, 0x80000
	s_addc_u32 s25, s25, 0
	s_add_u32 s26, s26, 0x80000
	s_addc_u32 s27, s27, 0
	global_store_dword v39, v60, s[20:21] sc1
	global_store_dword v39, v61, s[22:23] sc1
	global_store_dword v39, v62, s[24:25] sc1
	global_store_dword v39, v63, s[26:27] sc1
	s_add_u32 s20, s20, 0x80000
	s_addc_u32 s21, s21, 0
	s_add_u32 s22, s22, 0x80000
	s_addc_u32 s23, s23, 0
	s_add_u32 s24, s24, 0x80000
	s_addc_u32 s25, s25, 0
	s_add_u32 s26, s26, 0x80000
	s_addc_u32 s27, s27, 0
	global_store_dword v39, v64, s[20:21] sc1
	global_store_dword v39, v65, s[22:23] sc1
	global_store_dword v39, v66, s[24:25] sc1
	global_store_dword v39, v67, s[26:27] sc1
	s_add_u32 s20, s20, 0x80000
	s_addc_u32 s21, s21, 0
	s_add_u32 s22, s22, 0x80000
	s_addc_u32 s23, s23, 0
	s_add_u32 s24, s24, 0x80000
	s_addc_u32 s25, s25, 0
	s_add_u32 s26, s26, 0x80000
	s_addc_u32 s27, s27, 0
	global_store_dword v39, v68, s[20:21] sc1
	global_store_dword v39, v69, s[22:23] sc1
	global_store_dword v39, v70, s[24:25] sc1
	global_store_dword v39, v71, s[26:27] sc1
	s_add_u32 s20, s20, 0x80000
	s_addc_u32 s21, s21, 0
	s_add_u32 s22, s22, 0x80000
	s_addc_u32 s23, s23, 0
	s_add_u32 s24, s24, 0x80000
	s_addc_u32 s25, s25, 0
	s_add_u32 s26, s26, 0x80000
	s_addc_u32 s27, s27, 0
	global_store_dword v39, v72, s[20:21] sc1
	global_store_dword v39, v73, s[22:23] sc1
	global_store_dword v39, v74, s[24:25] sc1
	global_store_dword v39, v75, s[26:27] sc1
	s_add_u32 s20, s20, 0x80000
	s_addc_u32 s21, s21, 0
	s_add_u32 s22, s22, 0x80000
	s_addc_u32 s23, s23, 0
	s_add_u32 s24, s24, 0x80000
	s_addc_u32 s25, s25, 0
	s_add_u32 s26, s26, 0x80000
	s_addc_u32 s27, s27, 0
	global_store_dword v39, v76, s[20:21] sc1
	global_store_dword v39, v77, s[22:23] sc1
	global_store_dword v39, v78, s[24:25] sc1
	global_store_dword v39, v79, s[26:27] sc1
	s_add_u32 s20, s20, 0x80000
	s_addc_u32 s21, s21, 0
	s_add_u32 s22, s22, 0x80000
	s_addc_u32 s23, s23, 0
	s_add_u32 s24, s24, 0x80000
	s_addc_u32 s25, s25, 0
	s_add_u32 s26, s26, 0x80000
	s_addc_u32 s27, s27, 0
	global_store_dword v39, v80, s[20:21] sc1
	global_store_dword v39, v81, s[22:23] sc1
	global_store_dword v39, v82, s[24:25] sc1
	global_store_dword v39, v83, s[26:27] sc1
	s_add_u32 s20, s20, 0x80000
	s_addc_u32 s21, s21, 0
	s_add_u32 s22, s22, 0x80000
	s_addc_u32 s23, s23, 0
	s_add_u32 s24, s24, 0x80000
	s_addc_u32 s25, s25, 0
	s_add_u32 s26, s26, 0x80000
	s_addc_u32 s27, s27, 0
	global_store_dword v39, v84, s[20:21] sc1
	global_store_dword v39, v85, s[22:23] sc1
	global_store_dword v39, v86, s[24:25] sc1
	global_store_dword v39, v87, s[26:27] sc1
	s_add_u32 s20, s20, 0x80000
	s_addc_u32 s21, s21, 0
	s_add_u32 s22, s22, 0x80000
	s_addc_u32 s23, s23, 0
	s_add_u32 s24, s24, 0x80000
	s_addc_u32 s25, s25, 0
	s_add_u32 s26, s26, 0x80000
	s_addc_u32 s27, s27, 0
	global_store_dword v39, v88, s[20:21] sc1
	global_store_dword v39, v89, s[22:23] sc1
	global_store_dword v39, v90, s[24:25] sc1
	global_store_dword v39, v91, s[26:27] sc1
	s_add_u32 s20, s20, 0x80000
	s_addc_u32 s21, s21, 0
	s_add_u32 s22, s22, 0x80000
	s_addc_u32 s23, s23, 0
	s_add_u32 s24, s24, 0x80000
	s_addc_u32 s25, s25, 0
	s_add_u32 s26, s26, 0x80000
	s_addc_u32 s27, s27, 0
	global_store_dword v39, v92, s[20:21] sc1
	global_store_dword v39, v93, s[22:23] sc1
	global_store_dword v39, v94, s[24:25] sc1
	global_store_dword v39, v95, s[26:27] sc1
	s_add_u32 s20, s20, 0x80000
	s_addc_u32 s21, s21, 0
	s_add_u32 s22, s22, 0x80000
	s_addc_u32 s23, s23, 0
	s_add_u32 s24, s24, 0x80000
	s_addc_u32 s25, s25, 0
	s_add_u32 s26, s26, 0x80000
	s_addc_u32 s27, s27, 0
	global_store_dword v39, v96, s[20:21] sc1
	global_store_dword v39, v97, s[22:23] sc1
	global_store_dword v39, v98, s[24:25] sc1
	global_store_dword v39, v99, s[26:27] sc1
	s_add_u32 s20, s20, 0x80000
	s_addc_u32 s21, s21, 0
	s_add_u32 s22, s22, 0x80000
	s_addc_u32 s23, s23, 0
	s_add_u32 s24, s24, 0x80000
	s_addc_u32 s25, s25, 0
	s_add_u32 s26, s26, 0x80000
	s_addc_u32 s27, s27, 0
	global_store_dword v39, v100, s[20:21] sc1
	global_store_dword v39, v101, s[22:23] sc1
	global_store_dword v39, v102, s[24:25] sc1
	global_store_dword v39, v103, s[26:27] sc1
	s_add_u32 s20, s20, 0x80000
	s_addc_u32 s21, s21, 0
	s_add_u32 s22, s22, 0x80000
	s_addc_u32 s23, s23, 0
	s_add_u32 s24, s24, 0x80000
	s_addc_u32 s25, s25, 0
	s_add_u32 s26, s26, 0x80000
	s_addc_u32 s27, s27, 0
	global_store_dword v39, v104, s[20:21] sc1
	global_store_dword v39, v105, s[22:23] sc1
	global_store_dword v39, v106, s[24:25] sc1
	global_store_dword v39, v107, s[26:27] sc1
	s_add_u32 s20, s20, 0x80000
	s_addc_u32 s21, s21, 0
	s_add_u32 s22, s22, 0x80000
	s_addc_u32 s23, s23, 0
	s_add_u32 s24, s24, 0x80000
	s_addc_u32 s25, s25, 0
	s_add_u32 s26, s26, 0x80000
	s_addc_u32 s27, s27, 0
	global_store_dword v39, v108, s[20:21] sc1
	global_store_dword v39, v109, s[22:23] sc1
	global_store_dword v39, v110, s[24:25] sc1
	global_store_dword v39, v111, s[26:27] sc1
	s_add_u32 s20, s20, 0x80000
	s_addc_u32 s21, s21, 0
	s_add_u32 s22, s22, 0x80000
	s_addc_u32 s23, s23, 0
	s_add_u32 s24, s24, 0x80000
	s_addc_u32 s25, s25, 0
	s_add_u32 s26, s26, 0x80000
	s_addc_u32 s27, s27, 0
	global_store_dword v39, v112, s[20:21] sc1
	global_store_dword v39, v113, s[22:23] sc1
	global_store_dword v39, v114, s[24:25] sc1
	global_store_dword v39, v115, s[26:27] sc1
	s_add_u32 s20, s20, 0x80000
	s_addc_u32 s21, s21, 0
	s_add_u32 s22, s22, 0x80000
	s_addc_u32 s23, s23, 0
	s_add_u32 s24, s24, 0x80000
	s_addc_u32 s25, s25, 0
	s_add_u32 s26, s26, 0x80000
	s_addc_u32 s27, s27, 0
	global_store_dword v39, v116, s[20:21] sc1
	global_store_dword v39, v117, s[22:23] sc1
	global_store_dword v39, v118, s[24:25] sc1
	global_store_dword v39, v119, s[26:27] sc1
	s_add_u32 s20, s20, 0x80000
	s_addc_u32 s21, s21, 0
	s_add_u32 s22, s22, 0x80000
	s_addc_u32 s23, s23, 0
	s_add_u32 s24, s24, 0x80000
	s_addc_u32 s25, s25, 0
	s_add_u32 s26, s26, 0x80000
	s_addc_u32 s27, s27, 0
	global_store_dword v39, v120, s[20:21] sc1
	global_store_dword v39, v121, s[22:23] sc1
	global_store_dword v39, v122, s[24:25] sc1
	global_store_dword v39, v123, s[26:27] sc1
	s_add_u32 s20, s20, 0x80000
	s_addc_u32 s21, s21, 0
	s_add_u32 s22, s22, 0x80000
	s_addc_u32 s23, s23, 0
	s_add_u32 s24, s24, 0x80000
	s_addc_u32 s25, s25, 0
	s_add_u32 s26, s26, 0x80000
	s_addc_u32 s27, s27, 0
	global_store_dword v39, v124, s[20:21] sc1
	global_store_dword v39, v125, s[22:23] sc1
	global_store_dword v39, v126, s[24:25] sc1
	global_store_dword v39, v127, s[26:27] sc1
	s_add_u32 s20, s20, 0x80000
	s_addc_u32 s21, s21, 0
	s_add_u32 s22, s22, 0x80000
	s_addc_u32 s23, s23, 0
	s_add_u32 s24, s24, 0x80000
	s_addc_u32 s25, s25, 0
	s_add_u32 s26, s26, 0x80000
	s_addc_u32 s27, s27, 0
	global_store_dword v39, v36, s[20:21] sc1
	global_store_dword v39, v37, s[22:23] sc1
	global_store_dword v39, v45, s[24:25] sc1
	global_store_dword v39, v46, s[26:27] sc1
	s_add_u32 s20, s20, 0x80000
	s_addc_u32 s21, s21, 0
	s_add_u32 s22, s22, 0x80000
	s_addc_u32 s23, s23, 0
	s_add_u32 s24, s24, 0x80000
	s_addc_u32 s25, s25, 0
	s_add_u32 s26, s26, 0x80000
	s_addc_u32 s27, s27, 0
	global_store_dword v39, v53, s[20:21] sc1
	global_store_dword v39, v54, s[22:23] sc1
	global_store_dword v39, v55, s[24:25] sc1
	global_store_dword v39, v1, s[26:27] sc1
	s_add_u32 s20, s20, 0x80000
	s_addc_u32 s21, s21, 0
	s_add_u32 s22, s22, 0x80000
	s_addc_u32 s23, s23, 0
	s_add_u32 s24, s24, 0x80000
	s_addc_u32 s25, s25, 0
	s_add_u32 s26, s26, 0x80000
	s_addc_u32 s27, s27, 0
	ds_read_b128 v[56:59], v38 offset:4096
	ds_read_b128 v[60:63], v38 offset:5120
	ds_read_b128 v[64:67], v38 offset:6144
	ds_read_b128 v[68:71], v38 offset:7168
	s_waitcnt lgkmcnt(0)
	global_store_dword v39, v56, s[20:21] sc1
	global_store_dword v39, v57, s[22:23] sc1
	global_store_dword v39, v58, s[24:25] sc1
	global_store_dword v39, v59, s[26:27] sc1
	s_add_u32 s20, s20, 0x80000
	s_addc_u32 s21, s21, 0
	s_add_u32 s22, s22, 0x80000
	s_addc_u32 s23, s23, 0
	s_add_u32 s24, s24, 0x80000
	s_addc_u32 s25, s25, 0
	s_add_u32 s26, s26, 0x80000
	s_addc_u32 s27, s27, 0
	global_store_dword v39, v60, s[20:21] sc1
	global_store_dword v39, v61, s[22:23] sc1
	global_store_dword v39, v62, s[24:25] sc1
	global_store_dword v39, v63, s[26:27] sc1
	s_add_u32 s20, s20, 0x80000
	s_addc_u32 s21, s21, 0
	s_add_u32 s22, s22, 0x80000
	s_addc_u32 s23, s23, 0
	s_add_u32 s24, s24, 0x80000
	s_addc_u32 s25, s25, 0
	s_add_u32 s26, s26, 0x80000
	s_addc_u32 s27, s27, 0
	global_store_dword v39, v64, s[20:21] sc1
	global_store_dword v39, v65, s[22:23] sc1
	global_store_dword v39, v66, s[24:25] sc1
	global_store_dword v39, v67, s[26:27] sc1
	s_add_u32 s20, s20, 0x80000
	s_addc_u32 s21, s21, 0
	s_add_u32 s22, s22, 0x80000
	s_addc_u32 s23, s23, 0
	s_add_u32 s24, s24, 0x80000
	s_addc_u32 s25, s25, 0
	s_add_u32 s26, s26, 0x80000
	s_addc_u32 s27, s27, 0
	global_store_dword v39, v68, s[20:21] sc1
	global_store_dword v39, v69, s[22:23] sc1
	global_store_dword v39, v70, s[24:25] sc1
	global_store_dword v39, v71, s[26:27] sc1
	s_cmp_eq_u32 s29, 1
	s_cbranch_scc0 .Lk1_no24st
	s_add_u32 s20, s20, 0x80000
	s_addc_u32 s21, s21, 0
	s_add_u32 s22, s22, 0x80000
	s_addc_u32 s23, s23, 0
	s_add_u32 s24, s24, 0x80000
	s_addc_u32 s25, s25, 0
	s_add_u32 s26, s26, 0x80000
	s_addc_u32 s27, s27, 0
	global_store_dword v39, v18, s[20:21] sc1
	global_store_dword v39, v19, s[22:23] sc1
	global_store_dword v39, v20, s[24:25] sc1
	global_store_dword v39, v21, s[26:27] sc1
.Lk1_no24st:
	v_mul_f32_e32 v40, 0x3c010204, v40
	v_and_b32_e32 v42, 63, v0
	v_lshlrev_b32_e32 v41, 14, v42
	s_mov_b32 s15, s12
	s_lshl_b32 s15, s15, 2
	s_add_u32 s8, s8, s15
	s_addc_u32 s9, s9, 0
	s_add_u32 s15, s29, 24
	v_cmp_gt_u32_e32 vcc, s15, v42
	s_and_saveexec_b64 s[38:39], vcc
	global_store_dword v41, v40, s[8:9]
	s_mov_b64 exec, s[38:39]
	s_lshl_b32 s15, s14, 12
	v_add_u32_e32 v41, s15, v34
	s_barrier
	ds_write_b128 v41, v[2:5]
	ds_write_b128 v41, v[6:9] offset:1024
	ds_write_b128 v41, v[10:13] offset:2048
	ds_write_b128 v41, v[14:17] offset:3072
	s_waitcnt lgkmcnt(0)
	s_barrier
	s_movk_i32 s15, 0x100
	v_cmp_gt_u32_e32 vcc, s15, v0
	s_and_saveexec_b64 s[38:39], vcc
	s_cbranch_execz .Lk1_end
	v_lshlrev_b32_e32 v16, 4, v0
	ds_read_b128 v[2:5], v16
	ds_read_b128 v[18:21], v16 offset:4096
	ds_read_b128 v[22:25], v16 offset:8192
	ds_read_b128 v[26:29], v16 offset:12288
	ds_read_b128 v[30:33], v16 offset:16384
	ds_read_b128 v[34:37], v16 offset:20480
	ds_read_b128 v[38:41], v16 offset:24576
	ds_read_b128 v[42:45], v16 offset:28672
	s_waitcnt lgkmcnt(6)
	v_pk_add_f32 v[2:3], v[2:3], v[18:19]
	v_pk_add_f32 v[4:5], v[4:5], v[20:21]
	s_waitcnt lgkmcnt(5)
	v_pk_add_f32 v[2:3], v[2:3], v[22:23]
	v_pk_add_f32 v[4:5], v[4:5], v[24:25]
	s_waitcnt lgkmcnt(4)
	v_pk_add_f32 v[2:3], v[2:3], v[26:27]
	v_pk_add_f32 v[4:5], v[4:5], v[28:29]
	s_waitcnt lgkmcnt(3)
	v_pk_add_f32 v[2:3], v[2:3], v[30:31]
	v_pk_add_f32 v[4:5], v[4:5], v[32:33]
	s_waitcnt lgkmcnt(2)
	v_pk_add_f32 v[2:3], v[2:3], v[34:35]
	v_pk_add_f32 v[4:5], v[4:5], v[36:37]
	s_waitcnt lgkmcnt(1)
	v_pk_add_f32 v[2:3], v[2:3], v[38:39]
	v_pk_add_f32 v[4:5], v[4:5], v[40:41]
	s_waitcnt lgkmcnt(0)
	v_pk_add_f32 v[2:3], v[2:3], v[42:43]
	v_pk_add_f32 v[4:5], v[4:5], v[44:45]
	s_lshl_b32 s15, s2, 12
	s_add_u32 s10, s10, s15
	s_addc_u32 s11, s11, 0
	global_store_dwordx4 v16, v[2:5], s[10:11]
